# speedup vs baseline: 1.0068x; 1.0068x over previous
.Lno_anc:
	s_or_b64 exec, exec, s[8:9]
	v_mov_b32_e32 v7, 0x80
	s_and_b32 s27, s2, 0x78
	s_cmp_lg_u32 s27, 0
	s_cbranch_scc1 .Lno_touch
	v_lshlrev_b32_e32 v9, 4, v6
	s_mov_b64 exec, 1
	global_load_dword v48, v9, s[16:17] nt
	global_load_dword v49, v9, s[18:19] nt
	s_mov_b64 exec, -1
	s_waitcnt vmcnt(2)
	s_branch .Lmask_ready

.Lmask_ready:
	s_sub_u32 s26, 0xff, s2
	s_mul_i32 s26, s26, 0
	s_lshr_b32 s26, s26, 7
	s_min_u32 s26, s26, 64
	s_cmp_eq_u32 s26, 0
	s_cbranch_scc1 .Lhold_done

	.amdhsa_kernel _Z12giou_partialPK15HIP_vector_typeIfLj4EES2_S2_PKiPS_IfLj2EE
		.amdhsa_group_segment_fixed_size 49280
		.amdhsa_private_segment_fixed_size 0
		.amdhsa_kernarg_size 40
		.amdhsa_user_sgpr_count 2
		.amdhsa_user_sgpr_dispatch_ptr 0
		.amdhsa_user_sgpr_queue_ptr 0
		.amdhsa_user_sgpr_kernarg_segment_ptr 1
		.amdhsa_user_sgpr_dispatch_id 0
		.amdhsa_user_sgpr_kernarg_preload_length 0
		.amdhsa_user_sgpr_kernarg_preload_offset 0
		.amdhsa_user_sgpr_private_segment_size 0
		.amdhsa_uses_dynamic_stack 0
		.amdhsa_enable_private_segment 0
		.amdhsa_system_sgpr_workgroup_id_x 1
		.amdhsa_system_sgpr_workgroup_id_y 0
		.amdhsa_system_sgpr_workgroup_id_z 0
		.amdhsa_system_sgpr_workgroup_info 0
		.amdhsa_system_vgpr_workitem_id 0
		.amdhsa_next_free_vgpr 50
		.amdhsa_next_free_sgpr 34
		.amdhsa_accum_offset 52
		.amdhsa_reserve_vcc 1
		.amdhsa_float_round_mode_32 0
		.amdhsa_float_round_mode_16_64 0
		.amdhsa_float_denorm_mode_32 3
		.amdhsa_float_denorm_mode_16_64 3
		.amdhsa_dx10_clamp 1
		.amdhsa_ieee_mode 1
		.amdhsa_fp16_overflow 0
		.amdhsa_tg_split 0
		.amdhsa_exception_fp_ieee_invalid_op 0
		.amdhsa_exception_fp_denorm_src 0
		.amdhsa_exception_fp_ieee_div_zero 0
		.amdhsa_exception_fp_ieee_overflow 0
		.amdhsa_exception_fp_ieee_underflow 0
		.amdhsa_exception_fp_ieee_inexact 0
		.amdhsa_exception_int_div_zero 0
	.end_amdhsa_kernel

.Lfunc_end0:
	.size	_Z12giou_partialPK15HIP_vector_typeIfLj4EES2_S2_PKiPS_IfLj2EE, .Lfunc_end0-_Z12giou_partialPK15HIP_vector_typeIfLj4EES2_S2_PKiPS_IfLj2EE
	.set _Z12giou_partialPK15HIP_vector_typeIfLj4EES2_S2_PKiPS_IfLj2EE.num_vgpr, 50
	.set _Z12giou_partialPK15HIP_vector_typeIfLj4EES2_S2_PKiPS_IfLj2EE.num_agpr, 0
	.set _Z12giou_partialPK15HIP_vector_typeIfLj4EES2_S2_PKiPS_IfLj2EE.numbered_sgpr, 34
	.set _Z12giou_partialPK15HIP_vector_typeIfLj4EES2_S2_PKiPS_IfLj2EE.num_named_barrier, 0
	.set _Z12giou_partialPK15HIP_vector_typeIfLj4EES2_S2_PKiPS_IfLj2EE.private_seg_size, 0
	.set _Z12giou_partialPK15HIP_vector_typeIfLj4EES2_S2_PKiPS_IfLj2EE.uses_vcc, 1
	.set _Z12giou_partialPK15HIP_vector_typeIfLj4EES2_S2_PKiPS_IfLj2EE.uses_flat_scratch, 0
	.set _Z12giou_partialPK15HIP_vector_typeIfLj4EES2_S2_PKiPS_IfLj2EE.has_dyn_sized_stack, 0
	.set _Z12giou_partialPK15HIP_vector_typeIfLj4EES2_S2_PKiPS_IfLj2EE.has_recursion, 0
	.set _Z12giou_partialPK15HIP_vector_typeIfLj4EES2_S2_PKiPS_IfLj2EE.has_indirect_call, 0

amdhsa.kernels:
  - .agpr_count:     0
    .args:
      - .actual_access:  read_only
        .address_space:  global
        .offset:         0
        .size:           8
        .value_kind:     global_buffer
      - .actual_access:  read_only
        .address_space:  global
        .offset:         8
        .size:           8
        .value_kind:     global_buffer
      - .actual_access:  read_only
        .address_space:  global
        .offset:         16
        .size:           8
        .value_kind:     global_buffer
      - .actual_access:  read_only
        .address_space:  global
        .offset:         24
        .size:           8
        .value_kind:     global_buffer
      - .actual_access:  write_only
        .address_space:  global
        .offset:         32
        .size:           8
        .value_kind:     global_buffer
    .group_segment_fixed_size: 49280
    .kernarg_segment_align: 8
    .kernarg_segment_size: 40
    .language:       OpenCL C
    .language_version:
      - 2
      - 0
    .max_flat_workgroup_size: 1024
    .name:           _Z12giou_partialPK15HIP_vector_typeIfLj4EES2_S2_PKiPS_IfLj2EE
    .private_segment_fixed_size: 0
    .sgpr_count:     40
    .sgpr_spill_count: 0
    .symbol:         _Z12giou_partialPK15HIP_vector_typeIfLj4EES2_S2_PKiPS_IfLj2EE.kd
    .uniform_work_group_size: 1
    .uses_dynamic_stack: false
    .vgpr_count:     50
    .vgpr_spill_count: 0
    .wavefront_size: 64
  - .agpr_count:     0
    .args:
      - .actual_access:  read_only
        .address_space:  global
        .offset:         0
        .size:           8
        .value_kind:     global_buffer
      - .actual_access:  write_only
        .address_space:  global
        .offset:         8
        .size:           8
        .value_kind:     global_buffer
    .group_segment_fixed_size: 0
    .kernarg_segment_align: 8
    .kernarg_segment_size: 16
    .language:       OpenCL C
    .language_version:
      - 2
      - 0
    .max_flat_workgroup_size: 64
    .name:           _Z10giou_finalPK15HIP_vector_typeIfLj2EEPf
    .private_segment_fixed_size: 0
    .sgpr_count:     18
    .sgpr_spill_count: 0
    .symbol:         _Z10giou_finalPK15HIP_vector_typeIfLj2EEPf.kd
    .uniform_work_group_size: 1
    .uses_dynamic_stack: false
    .vgpr_count:     18
    .vgpr_spill_count: 0
    .wavefront_size: 64
